# v35
# speedup vs baseline: 1.0082x; 1.0003x over previous
.LBB0_10:
	s_or_b64 exec, exec, s[16:17]
	s_mov_b32 s3, 0xc3500
	v_cmp_gt_i32_e32 vcc, s3, v18
	s_waitcnt lgkmcnt(0)
	s_and_saveexec_b64 s[10:11], vcc
	s_cbranch_execz .LBB0_20
	v_mbcnt_lo_u32_b32 v1, -1, 0
	v_mbcnt_hi_u32_b32 v2, -1, v1
	v_and_b32_e32 v3, 64, v2
	v_xor_b32_e32 v1, 1, v2
	v_add_u32_e32 v3, 64, v3
	v_cmp_lt_i32_e32 vcc, v1, v3
	v_xor_b32_e32 v4, 2, v2
	s_lshl_b32 s24, s18, 11
	v_cndmask_b32_e32 v1, v2, v1, vcc
	v_cmp_lt_i32_e32 vcc, v4, v3
	s_add_i32 s14, s24, 0xfff80000
	v_ashrrev_i32_e32 v19, 31, v18
	v_cndmask_b32_e32 v4, v2, v4, vcc
	v_lshlrev_b32_e32 v24, 2, v4
	v_xor_b32_e32 v4, 4, v2
	v_cmp_lt_i32_e32 vcc, v4, v3
	s_lshl_b32 s25, s18, 12
	s_ashr_i32 s15, s14, 31
	v_cndmask_b32_e32 v4, v2, v4, vcc
	v_lshlrev_b32_e32 v25, 2, v4
	v_xor_b32_e32 v4, 8, v2
	v_cmp_lt_i32_e32 vcc, v4, v3
	v_lshlrev_b32_e32 v1, 2, v1
	s_add_i32 s24, s24, 0xfff00000
	v_cndmask_b32_e32 v2, v2, v4, vcc
	v_lshlrev_b32_e32 v26, 2, v2
	v_and_b32_e32 v2, 15, v0
	v_cmp_eq_u32_e64 s[6:7], 0, v2
	v_lshlrev_b32_e32 v2, 1, v0
	v_lshl_or_b32 v27, s2, 11, v2
	v_lshl_add_u64 v[2:3], v[18:19], 3, s[8:9]
	s_add_i32 s25, s25, 0xfff00000
	v_lshl_add_u64 v[20:21], v[2:3], 0, 4
	s_lshl_b64 s[16:17], s[14:15], 3
	s_lshl_b32 s15, s18, 10
	s_mov_b64 s[18:19], 0
	s_mov_b32 s26, 0x42fe0000
	s_movk_i32 s27, 0xff
	s_mov_b32 s28, 0xc34ff
	s_branch .LBB0_13

_Z3k_BPKiS0_PiS1_PKfPDF16_:
	v_cmp_eq_u32_e32 vcc, 0, v0
	s_and_saveexec_b64 s[4:5], vcc
	v_mov_b32_e32 v2, 0
	v_mov_b32_e32 v3, v2
	ds_write_b64 v2, v[2:3] offset:27712
	s_or_b64 exec, exec, s[4:5]
	s_load_dwordx2 s[24:25], s[0:1], 0x0
	s_load_dwordx4 s[36:39], s[0:1], 0x20
	s_movk_i32 s3, 0x100
	v_cmp_gt_u32_e32 vcc, s3, v0
	v_mbcnt_lo_u32_b32 v16, -1, 0
	v_and_b32_e32 v14, 63, v0
	s_waitcnt lgkmcnt(0)
	s_barrier
	s_lshl_b32 s40, s2, 11
	s_add_i32 s40, s40, 0xc3500
	v_add_u32_e32 v60, s40, v0
	v_min_u32_e32 v61, 0x1869ff, v60
	v_lshlrev_b32_e32 v61, 5, v61
	global_load_dwordx4 v[28:31], v61, s[36:37]
	global_load_dwordx4 v[32:35], v61, s[36:37] offset:16
	v_add_u32_e32 v62, 0x400, v60
	v_min_u32_e32 v61, 0x1869ff, v62
	v_lshlrev_b32_e32 v61, 5, v61
	global_load_dwordx4 v[36:39], v61, s[36:37]
	global_load_dwordx4 v[40:43], v61, s[36:37] offset:16
	s_and_saveexec_b64 s[6:7], vcc
	s_cbranch_execz .LBB1_12
	s_load_dwordx2 s[4:5], s[0:1], 0x8
	s_lshl_b32 s3, s2, 8
	v_or_b32_e32 v2, s3, v0
	s_addk_i32 s3, 0x100
	v_ashrrev_i32_e32 v3, 31, v2
	v_or_b32_e32 v4, s3, v0
	s_waitcnt lgkmcnt(0)
	v_lshl_add_u64 v[2:3], v[2:3], 2, s[4:5]
	v_ashrrev_i32_e32 v5, 31, v4
	v_lshl_add_u64 v[4:5], v[4:5], 2, s[4:5]
	global_load_dword v1, v[2:3], off
	global_load_dword v6, v[4:5], off
	v_mbcnt_hi_u32_b32 v2, -1, v16
	v_and_b32_e32 v3, 64, v2
	v_xor_b32_e32 v4, 32, v2
	v_add_u32_e32 v3, 64, v3
	v_cmp_lt_i32_e64 s[4:5], v4, v3
	v_xor_b32_e32 v7, 16, v2
	v_xor_b32_e32 v8, 8, v2
	v_cndmask_b32_e64 v4, v2, v4, s[4:5]
	v_lshlrev_b32_e32 v4, 2, v4
	v_cmp_lt_i32_e64 s[4:5], v7, v3
	v_xor_b32_e32 v9, 4, v2
	v_xor_b32_e32 v10, 2, v2
	v_cndmask_b32_e64 v7, v2, v7, s[4:5]
	v_lshlrev_b32_e32 v7, 2, v7
	v_cmp_lt_i32_e64 s[4:5], v8, v3
	v_xor_b32_e32 v11, 1, v2
	s_movk_i32 s3, 0x1870
	v_cndmask_b32_e64 v8, v2, v8, s[4:5]
	v_lshlrev_b32_e32 v8, 2, v8
	v_cmp_lt_i32_e64 s[4:5], v9, v3
	v_lshlrev_b32_e32 v5, 2, v0
	s_waitcnt vmcnt(1)
	ds_bpermute_b32 v12, v4, v1
	s_waitcnt vmcnt(0)
	v_sub_u32_e32 v6, v6, v1
	ds_bpermute_b32 v4, v4, v6
	v_cndmask_b32_e64 v9, v2, v9, s[4:5]
	v_lshlrev_b32_e32 v9, 2, v9
	s_waitcnt lgkmcnt(1)
	v_add_u32_e32 v12, v12, v1
	ds_bpermute_b32 v13, v7, v12
	s_waitcnt lgkmcnt(1)
	v_add_u32_e32 v4, v4, v6
	ds_bpermute_b32 v7, v7, v4
	v_cmp_lt_i32_e64 s[4:5], v10, v3
	s_waitcnt lgkmcnt(1)
	v_add_u32_e32 v12, v13, v12
	v_cndmask_b32_e64 v10, v2, v10, s[4:5]
	s_waitcnt lgkmcnt(0)
	v_add_u32_e32 v4, v7, v4
	ds_bpermute_b32 v7, v8, v12
	ds_bpermute_b32 v8, v8, v4
	v_lshlrev_b32_e32 v10, 2, v10
	v_cmp_lt_i32_e64 s[4:5], v11, v3
	s_waitcnt lgkmcnt(1)
	v_add_u32_e32 v7, v7, v12
	s_waitcnt lgkmcnt(0)
	v_add_u32_e32 v4, v8, v4
	ds_bpermute_b32 v8, v9, v7
	ds_bpermute_b32 v9, v9, v4
	v_cndmask_b32_e64 v2, v2, v11, s[4:5]
	v_lshlrev_b32_e32 v2, 2, v2
	v_cmp_eq_u32_e64 s[4:5], 0, v14
	s_waitcnt lgkmcnt(1)
	v_add_u32_e32 v7, v8, v7
	s_waitcnt lgkmcnt(0)
	v_add_u32_e32 v4, v9, v4
	ds_bpermute_b32 v8, v10, v7
	ds_bpermute_b32 v9, v10, v4
	v_mad_u32_u24 v10, v0, s3, v1
	ds_write2st64_b32 v5, v6, v10 offset0:96 offset1:100
	v_mov_b32_e32 v6, 0
	s_waitcnt lgkmcnt(2)
	v_add_u32_e32 v3, v8, v7
	s_waitcnt lgkmcnt(1)
	v_add_u32_e32 v1, v9, v4
	ds_bpermute_b32 v4, v2, v3
	ds_bpermute_b32 v2, v2, v1
	ds_write_b32 v5, v6 offset:26624
	s_and_b64 exec, exec, s[4:5]
	s_cbranch_execz .LBB1_12
	s_mov_b64 s[4:5], exec
	s_waitcnt lgkmcnt(2)
	v_add_u32_e32 v3, v4, v3
	s_mov_b32 s8, 0

.LBB1_12:
	s_or_b64 exec, exec, s[6:7]
	v_lshrrev_b32_e32 v1, 5, v0
	s_waitcnt lgkmcnt(2)
	v_lshlrev_b32_e32 v4, 2, v1
	s_waitcnt lgkmcnt(0)
	s_barrier
	s_waitcnt vmcnt(0)
	ds_read_b32 v24, v4 offset:24576
	v_and_b32_e32 v1, 31, v0
	v_or_b32_e32 v5, 0x6000, v4
	v_mov_b32_e32 v13, -1
	v_mov_b32_e32 v15, -1
	s_waitcnt lgkmcnt(0)
	v_cmp_lt_i32_e64 s[4:5], v1, v24
	s_and_saveexec_b64 s[6:7], s[4:5]
	s_cbranch_execz .LBB1_14
	ds_read_b32 v2, v4 offset:25600
	s_waitcnt lgkmcnt(0)
	v_add_u32_e32 v2, v2, v1
	v_ashrrev_i32_e32 v3, 31, v2
	v_lshl_add_u64 v[2:3], v[2:3], 2, s[24:25]
	global_load_dword v15, v[2:3], off

.LBB1_28:
	s_or_b64 exec, exec, s[6:7]
	s_mov_b64 s[52:53], vcc
	s_mov_b32 s41, 0x186a00
	v_cmp_gt_u32_e32 vcc, s41, v60
	s_and_saveexec_b64 s[42:43], vcc
	s_cbranch_execz .Lkb_cvv0
	v_max3_f32 v44, |v28|, 0, |v29|
	v_max3_f32 v44, v44, |v30|, |v31|
	v_max3_f32 v44, v44, |v32|, |v33|
	v_max3_f32 v44, v44, |v34|, |v35|
	s_nop 1
	v_max_f32_dpp v44, v44, v44 quad_perm:[1,0,3,2] row_mask:0xf bank_mask:0xf bound_ctrl:1
	s_nop 1
	v_max_f32_dpp v44, v44, v44 quad_perm:[2,3,0,1] row_mask:0xf bank_mask:0xf bound_ctrl:1
	s_nop 1
	v_max_f32_dpp v44, v44, v44 row_half_mirror row_mask:0xf bank_mask:0xf bound_ctrl:1
	s_nop 1
	v_max_f32_dpp v44, v44, v44 row_mirror row_mask:0xf bank_mask:0xf bound_ctrl:1
	s_mov_b32 s44, 0x42fe0000
	v_div_scale_f32 v52, s[46:47], v44, v44, s44
	v_rcp_f32_e32 v53, v52
	v_div_scale_f32 v54, vcc, s44, v44, s44
	v_fma_f32 v55, -v52, v53, 1.0
	v_fmac_f32_e32 v53, v55, v53
	v_mul_f32_e32 v55, v54, v53
	v_fma_f32 v56, -v52, v55, v54
	v_fmac_f32_e32 v55, v56, v53
	v_fma_f32 v52, -v52, v55, v54
	v_div_fmas_f32 v52, v52, v53, v55
	v_div_fixup_f32 v52, v52, v44, s44
	v_cmp_lt_f32_e32 vcc, 0, v44
	s_nop 1
	v_cndmask_b32_e32 v52, 0, v52, vcc
	v_mul_f32_e32 v28, v28, v52
	v_mul_f32_e32 v29, v29, v52
	v_mul_f32_e32 v30, v30, v52
	v_mul_f32_e32 v31, v31, v52
	v_mul_f32_e32 v32, v32, v52
	v_mul_f32_e32 v33, v33, v52
	v_mul_f32_e32 v34, v34, v52
	v_mul_f32_e32 v35, v35, v52
	v_rndne_f32_e32 v28, v28
	v_rndne_f32_e32 v29, v29
	v_rndne_f32_e32 v30, v30
	v_rndne_f32_e32 v31, v31
	v_rndne_f32_e32 v32, v32
	v_rndne_f32_e32 v33, v33
	v_rndne_f32_e32 v34, v34
	v_rndne_f32_e32 v35, v35
	v_add_f32_e32 v28, 0x43000000, v28
	v_add_f32_e32 v29, 0x43000000, v29
	v_add_f32_e32 v30, 0x43000000, v30
	v_add_f32_e32 v31, 0x43000000, v31
	v_add_f32_e32 v32, 0x43000000, v32
	v_add_f32_e32 v33, 0x43000000, v33
	v_add_f32_e32 v34, 0x43000000, v34
	v_add_f32_e32 v35, 0x43000000, v35
	v_cvt_pk_u8_f32 v46, v28, 0, 0
	v_cvt_pk_u8_f32 v47, v32, 0, 0
	v_cvt_pk_u8_f32 v46, v29, 1, v46
	v_cvt_pk_u8_f32 v47, v33, 1, v47
	v_cvt_pk_u8_f32 v46, v30, 2, v46
	v_cvt_pk_u8_f32 v47, v34, 2, v47
	v_cvt_pk_u8_f32 v46, v31, 3, v46
	v_cvt_pk_u8_f32 v47, v35, 3, v47
.Lkb_cvv0:
	s_mov_b64 exec, s[42:43]
	s_mov_b32 s41, 0x186a00
	v_cmp_gt_u32_e32 vcc, s41, v62
	s_and_saveexec_b64 s[42:43], vcc
	s_cbranch_execz .Lkb_cvv1
	v_max3_f32 v45, |v36|, 0, |v37|
	v_max3_f32 v45, v45, |v38|, |v39|
	v_max3_f32 v45, v45, |v40|, |v41|
	v_max3_f32 v45, v45, |v42|, |v43|
	s_nop 1
	v_max_f32_dpp v45, v45, v45 quad_perm:[1,0,3,2] row_mask:0xf bank_mask:0xf bound_ctrl:1
	s_nop 1
	v_max_f32_dpp v45, v45, v45 quad_perm:[2,3,0,1] row_mask:0xf bank_mask:0xf bound_ctrl:1
	s_nop 1
	v_max_f32_dpp v45, v45, v45 row_half_mirror row_mask:0xf bank_mask:0xf bound_ctrl:1
	s_nop 1
	v_max_f32_dpp v45, v45, v45 row_mirror row_mask:0xf bank_mask:0xf bound_ctrl:1
	s_mov_b32 s44, 0x42fe0000
	v_div_scale_f32 v52, s[46:47], v45, v45, s44
	v_rcp_f32_e32 v53, v52
	v_div_scale_f32 v54, vcc, s44, v45, s44
	v_fma_f32 v55, -v52, v53, 1.0
	v_fmac_f32_e32 v53, v55, v53
	v_mul_f32_e32 v55, v54, v53
	v_fma_f32 v56, -v52, v55, v54
	v_fmac_f32_e32 v55, v56, v53
	v_fma_f32 v52, -v52, v55, v54
	v_div_fmas_f32 v52, v52, v53, v55
	v_div_fixup_f32 v52, v52, v45, s44
	v_cmp_lt_f32_e32 vcc, 0, v45
	s_nop 1
	v_cndmask_b32_e32 v52, 0, v52, vcc
	v_mul_f32_e32 v36, v36, v52
	v_mul_f32_e32 v37, v37, v52
	v_mul_f32_e32 v38, v38, v52
	v_mul_f32_e32 v39, v39, v52
	v_mul_f32_e32 v40, v40, v52
	v_mul_f32_e32 v41, v41, v52
	v_mul_f32_e32 v42, v42, v52
	v_mul_f32_e32 v43, v43, v52
	v_rndne_f32_e32 v36, v36
	v_rndne_f32_e32 v37, v37
	v_rndne_f32_e32 v38, v38
	v_rndne_f32_e32 v39, v39
	v_rndne_f32_e32 v40, v40
	v_rndne_f32_e32 v41, v41
	v_rndne_f32_e32 v42, v42
	v_rndne_f32_e32 v43, v43
	v_add_f32_e32 v36, 0x43000000, v36
	v_add_f32_e32 v37, 0x43000000, v37
	v_add_f32_e32 v38, 0x43000000, v38
	v_add_f32_e32 v39, 0x43000000, v39
	v_add_f32_e32 v40, 0x43000000, v40
	v_add_f32_e32 v41, 0x43000000, v41
	v_add_f32_e32 v42, 0x43000000, v42
	v_add_f32_e32 v43, 0x43000000, v43
	v_cvt_pk_u8_f32 v48, v36, 0, 0
	v_cvt_pk_u8_f32 v49, v40, 0, 0
	v_cvt_pk_u8_f32 v48, v37, 1, v48
	v_cvt_pk_u8_f32 v49, v41, 1, v49
	v_cvt_pk_u8_f32 v48, v38, 2, v48
	v_cvt_pk_u8_f32 v49, v42, 2, v49
	v_cvt_pk_u8_f32 v48, v39, 3, v48
	v_cvt_pk_u8_f32 v49, v43, 3, v49
.Lkb_cvv1:
	s_mov_b64 exec, s[42:43]
	s_mov_b64 vcc, s[52:53]
	s_waitcnt vmcnt(0)
	v_cmp_lt_i32_e64 s[14:15], -1, v15
	s_and_saveexec_b64 s[4:5], s[14:15]
	v_lshrrev_b32_e32 v2, 15, v15
	v_and_b32_e32 v2, 0x1fffc, v2
	v_mov_b32_e32 v3, 1
	ds_add_u32 v2, v3 offset:26624
	s_or_b64 exec, exec, s[4:5]
	s_load_dwordx4 s[20:23], s[0:1], 0x10
	v_or_b32_e32 v6, 32, v1
	v_cmp_lt_i32_e64 s[0:1], v6, v24
	s_and_saveexec_b64 s[4:5], s[0:1]
	s_cbranch_execz .LBB1_33
	ds_read_b32 v2, v4 offset:25600
	s_mov_b64 s[6:7], 0
	v_mov_b32_e32 v25, 1
	s_mov_b64 s[8:9], 0x80
	v_mov_b32_e32 v26, v6
	s_waitcnt lgkmcnt(0)
	v_add3_u32 v2, v2, v1, 32
	v_ashrrev_i32_e32 v3, 31, v2
	v_lshl_add_u64 v[2:3], v[2:3], 2, s[24:25]

.LBB1_90:
	s_or_b64 exec, exec, s[2:3]
	v_mov_b32_e32 v2, 0
	s_waitcnt lgkmcnt(0)
	s_barrier
	s_add_u32 s48, s38, 0x30f4200
	s_addc_u32 s49, s39, 0
	s_add_u32 s50, s38, 0x495e400
	s_addc_u32 s51, s39, 0
	s_mov_b32 s41, 0x186a00
	v_cmp_gt_u32_e32 vcc, s41, v60
	s_and_saveexec_b64 s[42:43], vcc
	s_cbranch_execz .Lkb_cvs0
	v_lshlrev_b32_e32 v52, 3, v60
	global_store_dwordx2 v52, v[46:47], s[48:49]
	v_and_b32_e32 v53, 15, v60
	v_cmp_eq_u32_e32 vcc, 0, v53
	s_and_b64 exec, exec, vcc
	s_cbranch_execz .Lkb_cvs0
	v_mul_f32_e32 v54, 0x41010204, v44
	v_lshrrev_b32_e32 v55, 4, v60
	v_lshlrev_b32_e32 v55, 2, v55
	global_store_dword v55, v54, s[50:51]
.Lkb_cvs0:
	s_mov_b64 exec, s[42:43]
	s_mov_b32 s41, 0x186a00
	v_cmp_gt_u32_e32 vcc, s41, v62
	s_and_saveexec_b64 s[42:43], vcc
	s_cbranch_execz .Lkb_cvs1
	v_lshlrev_b32_e32 v52, 3, v62
	global_store_dwordx2 v52, v[48:49], s[48:49]
	v_and_b32_e32 v53, 15, v62
	v_cmp_eq_u32_e32 vcc, 0, v53
	s_and_b64 exec, exec, vcc
	s_cbranch_execz .Lkb_cvs1
	v_mul_f32_e32 v54, 0x41010204, v45
	v_lshrrev_b32_e32 v55, 4, v62
	v_lshlrev_b32_e32 v55, 2, v55
	global_store_dword v55, v54, s[50:51]

.LBB1_186:
	s_endpgm
	s_nop 0
	s_nop 0
	s_nop 0
	s_nop 0
	s_nop 0
	s_nop 0
	s_nop 0
	s_nop 0
	s_nop 0
	s_nop 0
	s_nop 0
	s_nop 0
	s_nop 0
	s_nop 0
	s_nop 0
	s_nop 0
	s_nop 0
	s_nop 0
	s_nop 0
	s_nop 0
	s_nop 0
	s_nop 0
	s_nop 0
	s_nop 0
	s_nop 0
	s_nop 0
	s_nop 0
	s_nop 0
	s_nop 0
	s_nop 0
	s_nop 0
	s_nop 0
	s_nop 0
	s_nop 0
	s_nop 0
	s_nop 0
	s_nop 0
	s_nop 0
	s_nop 0
	s_nop 0
	s_nop 0
	s_nop 0
	s_nop 0
	s_nop 0
	s_nop 0
	s_nop 0
	s_nop 0
	s_endpgm

	.amdhsa_kernel _Z3k_BPKiS0_PiS1_PKfPDF16_
		.amdhsa_group_segment_fixed_size 27720
		.amdhsa_private_segment_fixed_size 0
		.amdhsa_kernarg_size 48
		.amdhsa_user_sgpr_count 2
		.amdhsa_user_sgpr_dispatch_ptr 0
		.amdhsa_user_sgpr_queue_ptr 0
		.amdhsa_user_sgpr_kernarg_segment_ptr 1
		.amdhsa_user_sgpr_dispatch_id 0
		.amdhsa_user_sgpr_kernarg_preload_length 0
		.amdhsa_user_sgpr_kernarg_preload_offset 0
		.amdhsa_user_sgpr_private_segment_size 0
		.amdhsa_uses_dynamic_stack 0
		.amdhsa_enable_private_segment 0
		.amdhsa_system_sgpr_workgroup_id_x 1
		.amdhsa_system_sgpr_workgroup_id_y 0
		.amdhsa_system_sgpr_workgroup_id_z 0
		.amdhsa_system_sgpr_workgroup_info 0
		.amdhsa_system_vgpr_workitem_id 0
		.amdhsa_next_free_vgpr 64
		.amdhsa_next_free_sgpr 54
		.amdhsa_accum_offset 64
		.amdhsa_reserve_vcc 1
		.amdhsa_float_round_mode_32 0
		.amdhsa_float_round_mode_16_64 0
		.amdhsa_float_denorm_mode_32 3
		.amdhsa_float_denorm_mode_16_64 3
		.amdhsa_dx10_clamp 1
		.amdhsa_ieee_mode 1
		.amdhsa_fp16_overflow 0
		.amdhsa_tg_split 0
		.amdhsa_exception_fp_ieee_invalid_op 0
		.amdhsa_exception_fp_denorm_src 0
		.amdhsa_exception_fp_ieee_div_zero 0
		.amdhsa_exception_fp_ieee_overflow 0
		.amdhsa_exception_fp_ieee_underflow 0
		.amdhsa_exception_fp_ieee_inexact 0
		.amdhsa_exception_int_div_zero 0
	.end_amdhsa_kernel

.Lfunc_end1:
	.size	_Z3k_BPKiS0_PiS1_PKfPDF16_, .Lfunc_end1-_Z3k_BPKiS0_PiS1_PKfPDF16_
	.set _Z3k_BPKiS0_PiS1_PKfPDF16_.num_vgpr, 64
	.set _Z3k_BPKiS0_PiS1_PKfPDF16_.num_agpr, 0
	.set _Z3k_BPKiS0_PiS1_PKfPDF16_.numbered_sgpr, 54
	.set _Z3k_BPKiS0_PiS1_PKfPDF16_.num_named_barrier, 0
	.set _Z3k_BPKiS0_PiS1_PKfPDF16_.private_seg_size, 0
	.set _Z3k_BPKiS0_PiS1_PKfPDF16_.uses_vcc, 1
	.set _Z3k_BPKiS0_PiS1_PKfPDF16_.uses_flat_scratch, 0
	.set _Z3k_BPKiS0_PiS1_PKfPDF16_.has_dyn_sized_stack, 0
	.set _Z3k_BPKiS0_PiS1_PKfPDF16_.has_recursion, 0
	.set _Z3k_BPKiS0_PiS1_PKfPDF16_.has_indirect_call, 0

amdhsa.kernels:
  - .agpr_count:     0
    .args:
      - .actual_access:  read_only
        .address_space:  global
        .offset:         0
        .size:           8
        .value_kind:     global_buffer
      - .actual_access:  read_only
        .address_space:  global
        .offset:         8
        .size:           8
        .value_kind:     global_buffer
      - .actual_access:  read_only
        .address_space:  global
        .offset:         16
        .size:           8
        .value_kind:     global_buffer
      - .actual_access:  read_only
        .address_space:  global
        .offset:         24
        .size:           8
        .value_kind:     global_buffer
      - .actual_access:  read_only
        .address_space:  global
        .offset:         32
        .size:           8
        .value_kind:     global_buffer
      - .actual_access:  read_only
        .address_space:  global
        .offset:         40
        .size:           8
        .value_kind:     global_buffer
      - .actual_access:  read_only
        .address_space:  global
        .offset:         48
        .size:           8
        .value_kind:     global_buffer
      - .actual_access:  write_only
        .address_space:  global
        .offset:         56
        .size:           8
        .value_kind:     global_buffer
      - .actual_access:  write_only
        .address_space:  global
        .offset:         64
        .size:           8
        .value_kind:     global_buffer
      - .actual_access:  write_only
        .address_space:  global
        .offset:         72
        .size:           8
        .value_kind:     global_buffer
      - .actual_access:  write_only
        .address_space:  global
        .offset:         80
        .size:           8
        .value_kind:     global_buffer
      - .actual_access:  write_only
        .address_space:  global
        .offset:         88
        .size:           8
        .value_kind:     global_buffer
      - .actual_access:  write_only
        .address_space:  global
        .offset:         96
        .size:           8
        .value_kind:     global_buffer
      - .actual_access:  write_only
        .address_space:  global
        .offset:         104
        .size:           8
        .value_kind:     global_buffer
      - .actual_access:  write_only
        .address_space:  global
        .offset:         112
        .size:           8
        .value_kind:     global_buffer
      - .actual_access:  write_only
        .address_space:  global
        .offset:         120
        .size:           8
        .value_kind:     global_buffer
      - .actual_access:  write_only
        .address_space:  global
        .offset:         128
        .size:           8
        .value_kind:     global_buffer
      - .offset:         136
        .size:           4
        .value_kind:     hidden_block_count_x
      - .offset:         140
        .size:           4
        .value_kind:     hidden_block_count_y
      - .offset:         144
        .size:           4
        .value_kind:     hidden_block_count_z
      - .offset:         148
        .size:           2
        .value_kind:     hidden_group_size_x
      - .offset:         150
        .size:           2
        .value_kind:     hidden_group_size_y
      - .offset:         152
        .size:           2
        .value_kind:     hidden_group_size_z
      - .offset:         154
        .size:           2
        .value_kind:     hidden_remainder_x
      - .offset:         156
        .size:           2
        .value_kind:     hidden_remainder_y
      - .offset:         158
        .size:           2
        .value_kind:     hidden_remainder_z
      - .offset:         176
        .size:           8
        .value_kind:     hidden_global_offset_x
      - .offset:         184
        .size:           8
        .value_kind:     hidden_global_offset_y
      - .offset:         192
        .size:           8
        .value_kind:     hidden_global_offset_z
      - .offset:         200
        .size:           2
        .value_kind:     hidden_grid_dims
    .group_segment_fixed_size: 27136
    .kernarg_segment_align: 8
    .kernarg_segment_size: 392
    .language:       OpenCL C
    .language_version:
      - 2
      - 0
    .max_flat_workgroup_size: 1024
    .name:           _Z3k_APKfPKiS2_S0_S0_S0_S0_PDF16_S3_S3_S3_PiS4_PhS5_PfS6_
    .private_segment_fixed_size: 0
    .sgpr_count:     40
    .sgpr_spill_count: 0
    .symbol:         _Z3k_APKfPKiS2_S0_S0_S0_S0_PDF16_S3_S3_S3_PiS4_PhS5_PfS6_.kd
    .uniform_work_group_size: 1
    .uses_dynamic_stack: false
    .vgpr_count:     48
    .vgpr_spill_count: 0
    .wavefront_size: 64
  - .agpr_count:     0
    .args:
      - .actual_access:  read_only
        .address_space:  global
        .offset:         0
        .size:           8
        .value_kind:     global_buffer
      - .actual_access:  read_only
        .address_space:  global
        .offset:         8
        .size:           8
        .value_kind:     global_buffer
      - .actual_access:  write_only
        .address_space:  global
        .offset:         16
        .size:           8
        .value_kind:     global_buffer
      - .actual_access:  write_only
        .address_space:  global
        .offset:         24
        .size:           8
        .value_kind:     global_buffer
      - .actual_access:  read_only
        .address_space:  global
        .offset:         32
        .size:           8
        .value_kind:     global_buffer
      - .actual_access:  read_only
        .address_space:  global
        .offset:         40
        .size:           8
        .value_kind:     global_buffer
    .group_segment_fixed_size: 27720
    .kernarg_segment_align: 8
    .kernarg_segment_size: 48
    .language:       OpenCL C
    .language_version:
      - 2
      - 0
    .max_flat_workgroup_size: 1024
    .name:           _Z3k_BPKiS0_PiS1_PKfPDF16_
    .private_segment_fixed_size: 0
    .sgpr_count:     60
    .sgpr_spill_count: 0
    .symbol:         _Z3k_BPKiS0_PiS1_PKfPDF16_.kd
    .uniform_work_group_size: 1
    .uses_dynamic_stack: false
    .vgpr_count:     64
    .vgpr_spill_count: 0
    .wavefront_size: 64
  - .agpr_count:     0
    .args:
      - .actual_access:  read_only
        .address_space:  global
        .offset:         0
        .size:           8
        .value_kind:     global_buffer
      - .actual_access:  read_only
        .address_space:  global
        .offset:         8
        .size:           8
        .value_kind:     global_buffer
      - .actual_access:  read_only
        .address_space:  global
        .offset:         16
        .size:           8
        .value_kind:     global_buffer
      - .actual_access:  read_only
        .address_space:  global
        .offset:         24
        .size:           8
        .value_kind:     global_buffer
      - .actual_access:  read_only
        .address_space:  global
        .offset:         32
        .size:           8
        .value_kind:     global_buffer
      - .actual_access:  read_only
        .address_space:  global
        .offset:         40
        .size:           8
        .value_kind:     global_buffer
      - .actual_access:  read_only
        .address_space:  global
        .offset:         48
        .size:           8
        .value_kind:     global_buffer
      - .actual_access:  write_only
        .address_space:  global
        .offset:         56
        .size:           8
        .value_kind:     global_buffer
      - .actual_access:  write_only
        .address_space:  global
        .offset:         64
        .size:           8
        .value_kind:     global_buffer
      - .actual_access:  write_only
        .address_space:  global
        .offset:         72
        .size:           8
        .value_kind:     global_buffer
    .group_segment_fixed_size: 30720
    .kernarg_segment_align: 8
    .kernarg_segment_size: 80
    .language:       OpenCL C
    .language_version:
      - 2
      - 0
    .max_flat_workgroup_size: 256
    .name:           _Z7k_layerILb1EEvPKvPKhPKfPKiS7_PKDF16_S5_PvPhPf
    .private_segment_fixed_size: 0
    .sgpr_count:     36
    .sgpr_spill_count: 0
    .symbol:         _Z7k_layerILb1EEvPKvPKhPKfPKiS7_PKDF16_S5_PvPhPf.kd
    .uniform_work_group_size: 1
    .uses_dynamic_stack: false
    .vgpr_count:     94
    .vgpr_spill_count: 0
    .wavefront_size: 64
  - .agpr_count:     0
    .args:
      - .actual_access:  read_only
        .address_space:  global
        .offset:         0
        .size:           8
        .value_kind:     global_buffer
      - .actual_access:  read_only
        .address_space:  global
        .offset:         8
        .size:           8
        .value_kind:     global_buffer
      - .actual_access:  read_only
        .address_space:  global
        .offset:         16
        .size:           8
        .value_kind:     global_buffer
      - .actual_access:  read_only
        .address_space:  global
        .offset:         24
        .size:           8
        .value_kind:     global_buffer
      - .actual_access:  read_only
        .address_space:  global
        .offset:         32
        .size:           8
        .value_kind:     global_buffer
      - .actual_access:  read_only
        .address_space:  global
        .offset:         40
        .size:           8
        .value_kind:     global_buffer
      - .actual_access:  read_only
        .address_space:  global
        .offset:         48
        .size:           8
        .value_kind:     global_buffer
      - .actual_access:  write_only
        .address_space:  global
        .offset:         56
        .size:           8
        .value_kind:     global_buffer
      - .actual_access:  read_only
        .address_space:  global
        .offset:         64
        .size:           8
        .value_kind:     global_buffer
      - .actual_access:  read_only
        .address_space:  global
        .offset:         72
        .size:           8
        .value_kind:     global_buffer
    .group_segment_fixed_size: 30720
    .kernarg_segment_align: 8
    .kernarg_segment_size: 80
    .language:       OpenCL C
    .language_version:
      - 2
      - 0
    .max_flat_workgroup_size: 256
    .name:           _Z7k_layerILb0EEvPKvPKhPKfPKiS7_PKDF16_S5_PvPhPf
    .private_segment_fixed_size: 0
    .sgpr_count:     34
    .sgpr_spill_count: 0
    .symbol:         _Z7k_layerILb0EEvPKvPKhPKfPKiS7_PKDF16_S5_PvPhPf.kd
    .uniform_work_group_size: 1
    .uses_dynamic_stack: false
    .vgpr_count:     92
    .vgpr_spill_count: 0
    .wavefront_size: 64
